# speedup vs baseline: 1.0040x; 1.0040x over previous
.LBB0_30:
	s_setprio 2
	s_load_dwordx4 s[20:23], s[0:1], 0x28
	s_load_dwordx2 s[24:25], s[0:1], 0x38
	s_movk_i32 s2, 0x187
	v_cmp_gt_u32_e64 s[8:9], s2, v0
	s_and_saveexec_b64 s[4:5], s[8:9]
	s_cbranch_execz .LBB0_37
	s_movk_i32 s2, 0x87
	v_sub_u32_e64 v1, s2, v0 clamp
	v_add_u32_e32 v1, 0xff, v1
	v_lshrrev_b32_e32 v2, 8, v1
	s_movk_i32 s2, 0x620
	s_mov_b32 s6, 0
	v_mov_b32_e32 v1, v2
	v_lshl_add_u32 v3, v0, 2, s2
	s_mov_b32 s7, 1
	s_mov_b64 s[10:11], 0
	v_mov_b32_e32 v4, 0
	s_mov_b32 s12, s6
	s_branch .LBB0_33
